# s17 + s_setprio 1 for the x1 chunk-state waves while the pre-pass helper waves (cumsum, block means) share their SIMDs
# speedup vs baseline: 1.0119x; 1.0028x over previous
; __device__ __forceinline__ float shfl_idx(float x, int srclane) { return __int_as_float(__builtin_amdgcn_ds_bpermute(srclane << 2, __float_as_int(x))); }
; #define LFW(off) ((__attribute__((address_space(3))) float*)(R + W_SC + (off)))
; __device__ __forceinline__ void x1_wave(int item, int b0, const h16* __restrict__ proj, const float* __restrict__ small, const float* __restrict__ convw, ...
;     int lane = threadIdx.x & 63; (void)lane_in; asm volatile("" : "+v"(lane));
;     const int r32 = lane & 31, hi = lane >> 5;
;     const int c = item & 31, hh = (item >> 5) & 3, bl = item >> 7;
;     const size_t row0 = (size_t)bl * SEQ + c * 64;
;     const int gbh = (b0 + bl) * 4 + hh, lbh = bl * 4 + hh;
;     const int dg = lane & 15, rq = lane >> 4, isk = dg >> 3, pcol = isk ? 256 + hh * 64 + (dg - 8) * 8 : hh * 64 + dg * 8;
;     const float* sp = small + ((size_t)b0 * SEQ + row0 + lane) * 16;
;     const float li = sp[8 + hh], lf = sp[12 + hh];
;     const h16* vp = proj + row0 * PP + PC_CV + hh * 128 + (size_t)(lane >> 2) * PP + (lane & 3) * 8;
;     h16x8 xv[4][4];
; #pragma unroll
;     for (int sg = 0; sg < 4; ++sg)
; #pragma unroll
;         for (int vb = 0; vb < 4; ++vb) xv[sg][vb] = *(const h16x8*)(vp + (size_t)(16 * sg) * PP + 32 * vb);
;     h16x8 xin[19];
;     {   const int tl0 = c * 64 + rq * 16 - 3;
;         const h16* xp = proj + (size_t)bl * SEQ * PP + PC_CQK + pcol;
; #pragma unroll
;         for (int r = 0; r < 19; ++r) { const int tt = tl0 + r; xin[r] = *(const h16x8*)(xp + (size_t)(tt < 0 ? 0 : tt) * PP); }
;     }
;     f32x4 wq[4][2];
; #pragma unroll
;     for (int j = 0; j < 4; ++j) { wq[j][0] = *(const f32x4*)(convw + j * 512 + pcol); wq[j][1] = *(const f32x4*)(convw + j * 512 + pcol + 4); }
;     asm volatile("" ::: "memory");
;     {   float bc = lf;
; #pragma unroll
;         for (int o = 1; o < 64; o <<= 1) { const float u = shfl_idx(bc, lane - o); if (lane >= o) bc += u; }
;         const float as = li - bc; float mx = as;
; #pragma unroll
;         for (int o = 1; o < 64; o <<= 1) mx = fmaxf(mx, shfl_idx(mx, lane ^ o));
;         LFW(0)[lane] = __expf(as - mx);
;         if (lane == 63) { amax[gbh * 32 + c] = mx; blast[gbh * 32 + c] = bc; } }
.LBB0_882:
	s_setprio 1
	s_ashr_i32 s20, s6, 7
	s_add_i32 s0, s20, s4
	v_mov_b32_e32 v174, v250
	s_bfe_u32 s13, s6, 0x20005
	s_lshl_b32 s0, s0, 2
	s_waitcnt lgkmcnt(0)
	s_and_b32 s12, s6, 31
	s_ashr_i32 s21, s20, 31
	s_or_b32 s14, s0, s13
	v_and_b32_e32 v178, 15, v174
	s_lshl_b32 s0, s13, 6
	s_lshl_b64 s[40:41], s[20:21], 11
	s_lshl_b32 s15, s12, 6
	v_lshlrev_b32_e32 v0, 3, v178
	s_add_i32 s1, s0, 0xc0
	s_or_b32 s40, s40, s15
	v_add_u32_e32 v1, s1, v0
	v_or_b32_e32 v0, s0, v0
	v_readlane_b32 s0, v255, 43
	s_add_u32 s0, s40, s0
	v_cmp_gt_u32_e32 vcc, 8, v178
	s_addc_u32 s1, s41, 0
	v_ashrrev_i32_e32 v175, 31, v174
	v_cndmask_b32_e32 v42, v1, v0, vcc
	v_lshl_add_u64 v[0:1], s[0:1], 0, v[174:175]
	v_lshlrev_b64 v[0:1], 6, v[0:1]
	v_lshl_add_u64 v[0:1], s[86:87], 0, v[0:1]
	s_lshl_b32 s28, s13, 2
	v_lshl_add_u64 v[0:1], v[0:1], 0, s[28:29]
	global_load_dword v28, v[0:1], off offset:48
	s_mul_i32 s0, s41, 0x3800
	s_mul_hi_u32 s1, s40, 0x3800
	s_add_i32 s1, s1, s0
	s_mul_i32 s0, s40, 0x3800
	s_add_u32 s0, s16, s0
	s_addc_u32 s1, s17, s1
	s_lshl_b32 s18, s13, 8
	s_add_u32 s0, s0, s18
	s_addc_u32 s1, s1, 0
	s_add_u32 s0, s0, 0x2400
	s_addc_u32 s1, s1, 0
	v_ashrrev_i32_e32 v4, 2, v174
	v_mov_b64_e32 v[2:3], s[0:1]
	v_mad_i64_i32 v[2:3], s[0:1], v4, s91, v[2:3]
	v_lshlrev_b32_e32 v4, 3, v174
	v_and_b32_e32 v179, 24, v4
	v_lshlrev_b32_e32 v96, 1, v179
	v_lshl_add_u64 v[4:5], v[2:3], 0, v[96:97]
	global_load_dwordx4 v[84:87], v[4:5], off
	global_load_dword v190, v[0:1], off offset:32
	global_load_dwordx4 v[98:101], v[4:5], off offset:64
	global_load_dwordx4 v[102:105], v[4:5], off offset:128
	v_add_co_u32_e64 v0, s[0:1], s96, v4
	v_lshlrev_b32_e32 v191, 2, v174
	s_nop 0
	v_addc_co_u32_e64 v1, s[0:1], 0, v5, s[0:1]
	s_mov_b32 s0, 0x70000
	s_nop 0
	v_add_co_u32_e64 v2, s[0:1], s0, v4
	global_load_dwordx4 v[106:109], v[4:5], off offset:192
	global_load_dwordx4 v[110:113], v[0:1], off
	v_addc_co_u32_e64 v3, s[0:1], 0, v5, s[0:1]
	s_mov_b32 s0, 0xa8000
	s_nop 0
	v_add_co_u32_e64 v4, s[0:1], s0, v4
	v_and_b32_e32 v176, -16, v174
	s_nop 0
	v_addc_co_u32_e64 v5, s[0:1], 0, v5, s[0:1]
	s_mul_i32 s0, s20, 0x1c00000
	v_add_u32_e32 v26, -4, v191
	s_mul_hi_i32 s1, s20, 0x1c00000
	s_add_u32 s0, s16, s0
	v_add_u32_e32 v14, s15, v176
	s_addc_u32 s1, s17, s1
	v_lshlrev_b32_e32 v96, 1, v42
	v_add_u32_e32 v43, -3, v14
	v_lshl_add_u64 v[6:7], s[0:1], 0, v[96:97]
	s_mov_b64 s[0:1], 0x2000
	v_max_i32_e32 v10, -1, v43
	v_add_u32_e32 v12, -1, v14
	v_max_i32_e32 v16, -4, v43
	v_max_i32_e32 v18, -5, v43
	v_max_i32_e32 v20, -6, v43
	v_max_i32_e32 v22, -7, v43
	v_max_i32_e32 v24, -8, v43
	v_lshl_add_u64 v[6:7], v[6:7], 0, s[0:1]
	v_max_i32_e32 v8, 0, v43
	v_add_u32_e32 v10, 1, v10
	v_max_i32_e32 v12, 0, v12
	v_max_i32_e32 v14, 0, v14
	v_add_u32_e32 v16, 4, v16
	v_add_u32_e32 v18, 5, v18
	v_add_u32_e32 v20, 6, v20
	v_add_u32_e32 v22, 7, v22
	v_add_u32_e32 v24, 8, v24
	v_mad_u64_u32 v[8:9], s[0:1], v8, s91, v[6:7]
	v_mad_u64_u32 v[10:11], s[0:1], v10, s91, v[6:7]
	v_mad_u64_u32 v[12:13], s[0:1], v12, s91, v[6:7]
	v_mad_u64_u32 v[14:15], s[0:1], v14, s91, v[6:7]
	v_mad_u64_u32 v[16:17], s[0:1], v16, s91, v[6:7]
	v_mad_u64_u32 v[18:19], s[0:1], v18, s91, v[6:7]
	v_mad_u64_u32 v[20:21], s[0:1], v20, s91, v[6:7]
	v_mad_u64_u32 v[22:23], s[0:1], v22, s91, v[6:7]
	s_waitcnt vmcnt(0)
	ds_bpermute_b32 v29, v26, v28
	v_max_i32_e32 v26, -9, v43
	v_add_u32_e32 v26, 9, v26
	v_mad_u64_u32 v[24:25], s[0:1], v24, s91, v[6:7]
	v_mad_u64_u32 v[26:27], s[0:1], v26, s91, v[6:7]
	s_waitcnt lgkmcnt(0)
	v_add_f32_e32 v29, v28, v29
	v_cmp_gt_i32_e64 s[0:1], 1, v174
	v_max_i32_e32 v34, -13, v43
	v_max_i32_e32 v36, -14, v43
	v_cndmask_b32_e64 v30, v29, v28, s[0:1]
	v_add_u32_e32 v28, -8, v191
	ds_bpermute_b32 v31, v28, v30
	v_max_i32_e32 v28, -10, v43
	v_add_u32_e32 v28, 10, v28
	v_mad_u64_u32 v[28:29], s[0:1], v28, s91, v[6:7]
	s_waitcnt lgkmcnt(0)
	v_add_f32_e32 v31, v30, v31
	v_cmp_gt_i32_e64 s[0:1], 2, v174
	v_max_i32_e32 v38, -15, v43
	v_max_i32_e32 v40, -16, v43
	v_cndmask_b32_e64 v32, v31, v30, s[0:1]
	v_add_u32_e32 v30, -16, v191
	ds_bpermute_b32 v33, v30, v32
	v_max_i32_e32 v30, -11, v43
	v_add_u32_e32 v30, 11, v30
	v_mad_u64_u32 v[30:31], s[0:1], v30, s91, v[6:7]
	s_waitcnt lgkmcnt(0)
; __device__ __forceinline__ float shfl_idx(float x, int srclane) { return __int_as_float(__builtin_amdgcn_ds_bpermute(srclane << 2, __float_as_int(x))); }
; #define LFW(off) ((__attribute__((address_space(3))) float*)(R + W_SC + (off)))
; __device__ __forceinline__ void x1_wave(int item, int b0, const h16* __restrict__ proj, const float* __restrict__ small, const float* __restrict__ convw, ...
;     ...
;         for (int vb = 0; vb < 4; ++vb) xv[sg][vb] = *(const h16x8*)(vp + (size_t)(16 * sg) * PP + 32 * vb);
;     h16x8 xin[19];
;     {   const int tl0 = c * 64 + rq * 16 - 3;
;         const h16* xp = proj + (size_t)bl * SEQ * PP + PC_CQK + pcol;
; #pragma unroll
;         for (int r = 0; r < 19; ++r) { const int tt = tl0 + r; xin[r] = *(const h16x8*)(xp + (size_t)(tt < 0 ? 0 : tt) * PP); }
;     }
;     f32x4 wq[4][2];
; #pragma unroll
;     for (int j = 0; j < 4; ++j) { wq[j][0] = *(const f32x4*)(convw + j * 512 + pcol); wq[j][1] = *(const f32x4*)(convw + j * 512 + pcol + 4); }
;     asm volatile("" ::: "memory");
;     {   float bc = lf;
; #pragma unroll
;         for (int o = 1; o < 64; o <<= 1) { const float u = shfl_idx(bc, lane - o); if (lane >= o) bc += u; }
;         const float as = li - bc; float mx = as;
; #pragma unroll
;         for (int o = 1; o < 64; o <<= 1) mx = fmaxf(mx, shfl_idx(mx, lane ^ o));
;         LFW(0)[lane] = __expf(as - mx);
;         if (lane == 63) { amax[gbh * 32 + c] = mx; blast[gbh * 32 + c] = bc; } }
	v_add_f32_e32 v33, v32, v33
	v_cmp_gt_i32_e64 s[0:1], 4, v174
	v_max_i32_e32 v44, 0xffffffef, v43
	v_add_u32_e32 v34, 13, v34
	v_cndmask_b32_e64 v177, v33, v32, s[0:1]
	v_subrev_u32_e32 v32, 32, v191
	ds_bpermute_b32 v192, v32, v177
	v_max_i32_e32 v32, -12, v43
	v_max_i32_e32 v43, 0xffffffee, v43
	v_add_u32_e32 v32, 12, v32
	v_add_u32_e32 v36, 14, v36
	v_add_u32_e32 v38, 15, v38
	v_add_u32_e32 v40, 16, v40
	v_add_u32_e32 v44, 17, v44
	v_add_u32_e32 v43, 18, v43
	v_mad_u64_u32 v[32:33], s[0:1], v32, s91, v[6:7]
	v_mad_u64_u32 v[34:35], s[0:1], v34, s91, v[6:7]
	v_mad_u64_u32 v[36:37], s[0:1], v36, s91, v[6:7]
	v_mad_u64_u32 v[38:39], s[0:1], v38, s91, v[6:7]
	v_mad_u64_u32 v[40:41], s[0:1], v40, s91, v[6:7]
	v_mad_u64_u32 v[180:181], s[0:1], v44, s91, v[6:7]
	v_mad_u64_u32 v[6:7], s[0:1], v43, s91, v[6:7]
	v_lshlrev_b32_e32 v182, 2, v42
	v_mov_b32_e32 v183, v97
	v_lshl_add_u64 v[42:43], s[2:3], 0, v[182:183]
	s_mov_b64 s[0:1], 0x1000
	v_lshl_add_u64 v[184:185], v[42:43], 0, s[0:1]
	s_movk_i32 s0, 0x1000
	v_add_co_u32_e64 v186, s[0:1], s0, v42
	v_cmp_lt_u32_e64 s[38:39], 7, v178
	s_nop 0
	v_addc_co_u32_e64 v187, s[0:1], 0, v43, s[0:1]
	s_mov_b64 s[0:1], 0x1800
	s_nop 0
	v_lshl_add_u64 v[188:189], v[42:43], 0, s[0:1]
	global_load_dwordx4 v[130:133], v[0:1], off offset:64
	global_load_dwordx4 v[134:137], v[0:1], off offset:128
	global_load_dwordx4 v[138:141], v[0:1], off offset:192
	global_load_dwordx4 v[142:145], v[2:3], off
	global_load_dwordx4 v[146:149], v[2:3], off offset:64
	global_load_dwordx4 v[150:153], v[2:3], off offset:128
	global_load_dwordx4 v[154:157], v[2:3], off offset:192
	global_load_dwordx4 v[158:161], v[4:5], off
	global_load_dwordx4 v[162:165], v[4:5], off offset:64
	global_load_dwordx4 v[166:169], v[4:5], off offset:128
	global_load_dwordx4 v[170:173], v[4:5], off offset:192
	global_load_dwordx4 v[126:129], v[8:9], off
	global_load_dwordx4 v[122:125], v[10:11], off
	global_load_dwordx4 v[118:121], v[12:13], off
	global_load_dwordx4 v[114:117], v[14:15], off
	global_load_dwordx4 v[92:95], v[16:17], off
	global_load_dwordx4 v[88:91], v[18:19], off
	global_load_dwordx4 v[80:83], v[20:21], off
	global_load_dwordx4 v[76:79], v[22:23], off
	global_load_dwordx4 v[72:75], v[24:25], off
	global_load_dwordx4 v[68:71], v[26:27], off
	global_load_dwordx4 v[64:67], v[28:29], off
	global_load_dwordx4 v[60:63], v[30:31], off
	global_load_dwordx4 v[56:59], v[32:33], off
	global_load_dwordx4 v[52:55], v[34:35], off
	global_load_dwordx4 v[48:51], v[36:37], off
	global_load_dwordx4 v[44:47], v[38:39], off
	s_nop 0
	global_load_dwordx4 v[40:43], v[40:41], off
	s_nop 0
	global_load_dwordx4 v[36:39], v[180:181], off
	s_nop 0
	global_load_dwordx4 v[4:7], v[6:7], off
	s_nop 0
	global_load_dwordx4 v[8:11], v182, s[2:3] offset:16
	global_load_dwordx4 v[24:27], v182, s[2:3]
	global_load_dwordx4 v[12:15], v182, s[2:3] offset:2064
	global_load_dwordx4 v[28:31], v182, s[2:3] offset:2048
	global_load_dwordx4 v[16:19], v[184:185], off offset:16
	global_load_dwordx4 v[32:35], v[186:187], off
	global_load_dwordx4 v[20:23], v[186:187], off offset:2048
	global_load_dwordx4 v[0:3], v[188:189], off offset:16
	s_waitcnt lgkmcnt(0)
	v_add_f32_e32 v180, v177, v192
	v_cmp_gt_i32_e64 s[0:1], 8, v174
	v_xor_b32_e32 v182, 8, v191
	s_nop 0
	v_cndmask_b32_e64 v177, v180, v177, s[0:1]
	v_subrev_u32_e32 v180, 64, v191
	ds_bpermute_b32 v180, v180, v177
	v_cmp_gt_i32_e64 s[0:1], 16, v174
	s_waitcnt lgkmcnt(0)
	v_add_f32_e32 v180, v177, v180
	v_cndmask_b32_e64 v180, v180, v177, s[0:1]
	v_add_u32_e32 v177, 0xffffff80, v191
	ds_bpermute_b32 v177, v177, v180
	v_cmp_gt_i32_e64 s[0:1], 32, v174
	s_waitcnt lgkmcnt(0)
	v_add_f32_e32 v177, v180, v177
	v_cndmask_b32_e64 v180, v177, v180, s[0:1]
	v_sub_f32_e32 v181, v190, v180
	v_xor_b32_e32 v180, 4, v191
	ds_bpermute_b32 v180, v180, v181
	v_cmp_eq_u32_e64 s[0:1], 63, v174
	s_waitcnt lgkmcnt(0)
	v_max_f32_e32 v180, v180, v180
	v_max_f32_e32 v180, v181, v180
	ds_bpermute_b32 v182, v182, v180
	s_waitcnt lgkmcnt(0)
	v_max_f32_e32 v182, v182, v182
	v_max_f32_e32 v180, v180, v182
	v_xor_b32_e32 v182, 16, v191
	ds_bpermute_b32 v182, v182, v180
	s_waitcnt lgkmcnt(0)
	v_max_f32_e32 v182, v182, v182
	v_max_f32_e32 v180, v180, v182
	v_xor_b32_e32 v182, 32, v191
	ds_bpermute_b32 v182, v182, v180
	s_waitcnt lgkmcnt(0)
	v_max_f32_e32 v182, v182, v182
	v_max_f32_e32 v180, v180, v182
	v_xor_b32_e32 v182, 64, v191
	ds_bpermute_b32 v182, v182, v180
	s_waitcnt lgkmcnt(0)
	v_max_f32_e32 v182, v182, v182
	v_max_f32_e32 v180, v180, v182
	v_xor_b32_e32 v182, 0x80, v191
	ds_bpermute_b32 v182, v182, v180
	s_waitcnt lgkmcnt(0)
	v_max_f32_e32 v182, v182, v182
	v_max_f32_e32 v180, v180, v182
	v_sub_f32_e32 v181, v181, v180
	v_mul_f32_e32 v181, 0x3fb8aa3b, v181
	v_exp_f32_e32 v181, v181
	v_add_u32_e32 v182, s10, v191
	ds_write_b32 v182, v181 offset:25088
	s_and_saveexec_b64 s[42:43], s[0:1]
	s_cbranch_execz .LBB0_884
	s_lshl_b32 s0, s14, 5
	s_or_b32 s0, s0, s12
	s_ashr_i32 s1, s0, 31
	s_lshl_b64 s[0:1], s[0:1], 2
	v_readlane_b32 s18, v254, 34
	v_readlane_b32 s19, v254, 35
	s_add_u32 s18, s18, s0
	s_addc_u32 s19, s19, s1
	v_readlane_b32 s26, v254, 32
	v_readlane_b32 s27, v254, 33
	s_add_u32 s0, s26, s0
	s_addc_u32 s1, s27, s1
	s_movk_i32 s27, 0x2000
	global_store_dword v97, v180, s[18:19]
	global_store_dword v97, v177, s[0:1]

; __global__ void __launch_bounds__(NTHREADS, 2) mega(MArgs a) {
;     ...
;                 if (wv < mlstm::NACT) for (int it = blockIdx.x * mlstm::NACT + wv; it < HB * 128; it += gridDim.x * mlstm::NACT)
;                     mlstm::x1_wave(it, b0, (const h16*)(ws + WS_PROJ), (const float*)(ws + WS_SMALL), a.in[4] + (size_t)layer * 4 * 512, (h16*)(ws + WS_QKC), (h16*)(ws + WS_U),
;                                    (float*)(ws + WS_MUN), (float*)(ws + WS_MAMAX), (float*)(ws + WS_MBLAST), (mlstm::lds_ptr)L + wv * mlstm::WREG, ln);
;                 if (wv >= mlstm::NACT) for (int wq = blockIdx.x * (NWAVES - mlstm::NACT) + (wv - mlstm::NACT); wq < HB * 8 + HB * 64; wq += gridDim.x * (NWAVES - mlstm::NACT)) {
;                     if (wq < HB * 8) fox_cumsum_wave(wq, b0, (const float*)(ws + WS_SMALL), (float*)(ws + WS_CB));
;                     else moba_kmean_wave(wq - HB * 8, b0, (const h16*)(ws + WS_PROJ), (float*)(ws + WS_KMEAN)); }
.LBB0_922:
	s_setprio 0
	s_cmp_lt_i32 s5, 4
	v_readlane_b32 s2, v254, 37
	s_cselect_b64 s[0:1], -1, 0
	s_add_i32 s2, s2, s5
	s_cmpk_gt_i32 s2, 0x23f
	s_cselect_b64 s[10:11], -1, 0
	s_or_b64 s[0:1], s[0:1], s[10:11]
	s_and_b64 vcc, exec, s[0:1]
	s_cbranch_vccz .LBB0_936
